# post0 rope: the two lane-class bodies of each step merged into one (partner fetched with its sign applied via v_xor_b32_dpp), checked by symbolic equivalence
# speedup vs baseline: 1.0002x; 1.0002x over previous
.LBB0_556:
	s_or_b64 exec, exec, s[2:3]
	v_ashrrev_i32_e32 v3, 6, v3
	v_lshl_add_u32 v94, s94, 3, v3
	s_movk_i32 s2, 0x4000
	v_cmp_gt_i32_e32 vcc, s2, v94
	s_and_saveexec_b64 s[18:19], vcc
	s_cbranch_execz .LBB0_831
	v_mbcnt_lo_u32_b32 v3, -1, 0
	v_mbcnt_hi_u32_b32 v3, -1, v3
	v_and_b32_e32 v5, 64, v3
	v_xor_b32_e32 v4, 1, v3
	v_add_u32_e32 v6, 64, v5
	v_cmp_lt_i32_e32 vcc, v4, v6
	v_and_b32_e32 v96, 7, v2
	v_and_b32_e32 v8, 15, v2
	v_cndmask_b32_e32 v4, v3, v4, vcc
	v_lshlrev_b32_e32 v208, 2, v4
	v_xor_b32_e32 v4, 2, v3
	v_cmp_lt_i32_e32 vcc, v4, v6
	v_mov_b32_e32 v99, 0
	s_mov_b64 s[2:3], 0x5ed10000
	v_cndmask_b32_e32 v4, v3, v4, vcc
	v_lshlrev_b32_e32 v209, 2, v4
	v_xor_b32_e32 v4, 4, v3
	v_cmp_lt_i32_e32 vcc, v4, v6
	v_readlane_b32 s64, v254, 2
	v_mov_b32_e32 v7, v99
	v_cndmask_b32_e32 v4, v3, v4, vcc
	v_lshlrev_b32_e32 v210, 2, v4
	v_and_b32_e32 v4, 48, v2
	v_cmp_eq_u32_e64 s[4:5], 16, v4
	v_xor_b32_e32 v4, 32, v3
	v_cmp_lt_i32_e32 vcc, v4, v6
	v_lshlrev_b32_e32 v2, 1, v2
	v_and_b32_e32 v215, 48, v2
	v_cndmask_b32_e32 v4, v3, v4, vcc
	v_lshlrev_b32_e32 v211, 2, v4
	v_xor_b32_e32 v4, 16, v3
	v_cmp_lt_i32_e32 vcc, v4, v6
	v_lshlrev_b32_e32 v2, 5, v1
	v_readlane_b32 s74, v254, 12
	v_cndmask_b32_e32 v4, v3, v4, vcc
	v_lshlrev_b32_e32 v212, 2, v4
	v_xor_b32_e32 v4, 8, v3
	v_cmp_lt_i32_e32 vcc, v4, v6
	v_or_b32_e32 v6, 0x1000, v2
	v_readlane_b32 s75, v254, 13
	v_cndmask_b32_e32 v4, v3, v4, vcc
	v_lshlrev_b32_e32 v213, 2, v4
	v_or_b32_e32 v4, v5, v96
	v_lshl_or_b32 v214, v4, 2, 64
	v_and_b32_e32 v4, 0x400, v2
	v_mov_b32_e32 v5, v99
	v_lshlrev_b32_e32 v3, 2, v3
	v_lshl_add_u64 v[4:5], s[88:89], 0, v[4:5]
	v_and_b32_e32 v216, 0x100, v3
	v_mov_b32_e32 v3, v99
	v_lshl_add_u64 v[100:101], v[4:5], 0, s[2:3]
	v_lshlrev_b32_e32 v4, 6, v96
	v_mov_b32_e32 v5, v99
	v_readlane_b32 s76, v254, 14
	v_readlane_b32 s77, v254, 15
	v_lshl_add_u64 v[110:111], s[48:49], 0, v[2:3]
	s_mov_b64 s[2:3], 0x4800
	v_lshl_add_u64 v[118:119], s[48:49], 0, v[6:7]
	v_ashrrev_i32_e32 v95, 31, v94
	v_lshl_add_u64 v[102:103], s[74:75], 0, v[4:5]
	v_lshl_add_u64 v[104:105], s[76:77], 0, v[4:5]
	v_lshlrev_b32_e32 v4, 2, v1
	v_lshl_add_u64 v[112:113], v[110:111], 0, s[2:3]
	v_lshl_add_u64 v[116:117], s[50:51], 0, v[6:7]
	v_lshl_add_u64 v[120:121], v[118:119], 0, s[2:3]
	s_mov_b64 s[2:3], 0x1800
	v_lshlrev_b64 v[6:7], 5, v[94:95]
	v_lshl_add_u64 v[124:125], v[110:111], 0, s[2:3]
	v_lshl_add_u64 v[132:133], v[118:119], 0, s[2:3]
	v_lshl_add_u64 v[6:7], v[6:7], 0, v[4:5]
	s_mov_b64 s[2:3], 0x5ef10000
	v_lshl_add_u64 v[140:141], v[6:7], 0, s[2:3]
	v_lshlrev_b64 v[6:7], 6, v[94:95]
	v_lshl_add_u64 v[6:7], v[6:7], 0, v[4:5]
	s_mov_b64 s[2:3], 0x5ef90000
	v_lshlrev_b32_e32 v10, 5, v8
	v_lshl_add_u64 v[142:143], v[6:7], 0, s[2:3]
	s_movk_i32 s2, 0xc00
	v_lshlrev_b32_e32 v9, 4, v96
	v_and_b32_e32 v11, 0x100, v10
	v_lshlrev_b64 v[138:139], 9, v[94:95]
	v_mad_i64_i32 v[144:145], s[2:3], v94, s2, 0
	v_lshlrev_b64 v[6:7], 10, v[94:95]
	v_readlane_b32 s78, v254, 16
	v_readlane_b32 s79, v254, 17
	v_or3_b32 v138, v138, v11, v9
	v_lshl_or_b32 v8, v8, 2, v6
	v_mov_b32_e32 v9, v7
	s_mov_b64 s[2:3], 0x59d10120
	v_lshl_add_u64 v[106:107], s[78:79], 0, v[4:5]
	s_mov_b64 s[8:9], 0x5000
	v_lshl_add_u64 v[122:123], s[52:53], 0, v[4:5]
	v_lshl_add_u64 v[148:149], v[8:9], 0, s[2:3]
	v_or_b32_e32 v4, v6, v4
	v_mov_b32_e32 v5, v7
	s_mov_b64 s[2:3], 0x59d10000
	v_lshlrev_b32_e32 v98, 4, v1
	v_lshl_add_u64 v[114:115], v[110:111], 0, s[8:9]
	s_mov_b64 s[8:9], 0x3000
	v_lshl_add_u64 v[150:151], v[4:5], 0, s[2:3]
	v_lshl_or_b32 v4, v96, 2, v6
	s_mov_b64 s[2:3], 0x59d10100
	s_lshl_b32 s20, s92, 3
	v_lshl_add_u64 v[126:127], v[110:111], 0, s[8:9]
	s_mov_b64 s[10:11], 0x2000
	v_lshl_add_u64 v[134:135], v[118:119], 0, s[8:9]
	v_lshl_add_u64 v[152:153], v[4:5], 0, s[2:3]
	v_or_b32_e32 v6, v6, v98
	s_mov_b64 s[2:3], 0x5dd10000
	s_movk_i32 s8, 0x2600
	v_readlane_b32 s65, v254, 3
	v_readlane_b32 s66, v254, 4
	v_readlane_b32 s67, v254, 5
	v_readlane_b32 s68, v254, 6
	v_readlane_b32 s69, v254, 7
	v_readlane_b32 s70, v254, 8
	v_readlane_b32 s71, v254, 9
	v_lshl_add_u64 v[128:129], v[110:111], 0, s[10:11]
	s_mov_b64 s[10:11], 0x3800
	s_ashr_i32 s21, s20, 31
	v_lshlrev_b64 v[146:147], 11, v[94:95]
	v_lshl_add_u64 v[154:155], v[6:7], 0, s[2:3]
	v_mad_i64_i32 v[156:157], s[2:3], v94, s8, 0
	v_cmp_gt_u32_e64 s[6:7], 8, v1
	v_or_b32_e32 v217, 4, v216
	v_or_b32_e32 v218, 8, v216
	v_or_b32_e32 v219, 12, v216
	v_or_b32_e32 v220, 16, v216
	v_or_b32_e32 v221, 20, v216
	v_or_b32_e32 v222, 24, v216
	v_or_b32_e32 v223, 28, v216
	v_or_b32_e32 v224, 32, v216
	v_or_b32_e32 v225, 36, v216
	v_or_b32_e32 v226, 40, v216
	v_or_b32_e32 v227, 44, v216
	v_or_b32_e32 v228, 48, v216
	v_or_b32_e32 v229, 52, v216
	v_or_b32_e32 v230, 56, v216
	v_or_b32_e32 v231, 60, v216
	v_or_b32_e32 v232, 64, v216
	v_or_b32_e32 v233, 0x44, v216
	v_or_b32_e32 v234, 0x48, v216
	v_or_b32_e32 v235, 0x4c, v216
	v_or_b32_e32 v236, 0x50, v216
	v_or_b32_e32 v237, 0x54, v216
	v_or_b32_e32 v238, 0x58, v216
	v_or_b32_e32 v239, 0x5c, v216
	v_lshl_add_u64 v[108:109], s[50:51], 0, v[2:3]
	v_lshl_add_u64 v[130:131], v[110:111], 0, s[10:11]
	v_lshl_add_u64 v[136:137], v[94:95], 2, s[66:67]
	s_lshl_b64 s[22:23], s[20:21], 2
	s_lshl_b64 s[24:25], s[20:21], 9
	s_lshl_b64 s[26:27], s[20:21], 5
	s_lshl_b64 s[28:29], s[20:21], 6
	v_or_b32_e32 v144, v144, v98
	s_mul_i32 s30, s92, 0x6000
	s_mul_hi_i32 s31, s20, 0xc00
	v_or_b32_e32 v146, v146, v2
	s_lshl_b64 s[34:35], s[20:21], 11
	s_lshl_b64 s[36:37], s[20:21], 10
	v_mad_i64_i32 v[158:159], s[2:3], v94, s8, v[98:99]
	s_mul_i32 s38, s92, 0x13000
	s_mul_hi_i32 s39, s20, 0x2600
	v_or_b32_e32 v156, v156, v10
	v_mad_i64_i32 v[160:161], s[2:3], v94, s8, v[2:3]
	s_mov_b64 s[40:41], 0
	s_mov_b64 s[42:43], 0x39d10000
	s_mov_b32 s21, 0x39d10000
	s_mov_b64 s[44:45], 0x39d10800
	s_mov_b64 s[46:47], 0x39d10a00
	s_mov_b32 s33, 0x39d11000
	s_mov_b32 s48, 0x39d12000
	s_brev_b32 s49, 18
	s_mov_b32 s50, 0x800000
	s_mov_b32 s51, 0xfe5163ab
	s_mov_b32 s52, 0x3c439041
	s_mov_b32 s53, 0xdb629599
	s_mov_b32 s60, 0xf534ddc0
	s_mov_b32 s61, 0xfc2757d1
	s_mov_b32 s62, 0x4e441529
	s_mov_b32 s63, 0xa2f9836e
	s_mov_b32 s64, 0x3fc90fda
	s_mov_b32 s65, 0x3f22f983
	s_mov_b32 s66, 0xbfc90fda
	s_brev_b32 s67, 1
	s_movk_i32 s68, 0x1f8
	v_mov_b32_e32 v95, 0x358637bd
	s_mov_b32 s69, 0x5ad10000
	v_lshlrev_b32_e32 v162, 1, v96
	s_mov_b32 s70, 0x41a00000
	s_mov_b32 s71, 0x3fb8aa3b
	s_mov_b32 s74, 0xc2ce8ed0
	s_mov_b32 s75, 0x42b17218
	s_mov_b32 s76, 0x7f800000
	s_mov_b32 s77, 0x3f2aaaab
	s_mov_b32 s78, 0x3f317218
	s_mov_b32 s79, 0x33800000
	s_mov_b32 s80, 0x5f090000
	v_mov_b32_e32 v243, 0xffff8e00
	v_mov_b32_e32 v246, 0xffffb400
	v_mov_b32_e32 v242, 0xffffda00
	v_not_b32_e32 v244, 31
	v_mov_b32_e32 v245, 0x7fc00000
	v_mov_b32_e32 v164, 0x3f317218
	s_movk_i32 s81, 0x3fff
	v_readlane_b32 s72, v254, 10
	v_readlane_b32 s73, v254, 11
	v_cmp_eq_u32_e64 s[82:83], 1, v96
	v_cmp_eq_u32_e64 s[84:85], 0, v96
	s_or_b64 s[86:87], s[82:83], s[84:85]
	v_bfrev_b32_e32 v208, 1
	s_nop 1
	v_cndmask_b32_e64 v208, 0, v208, s[84:85]
	s_branch .LBB0_559

.LBB0_561:
	s_andn2_saveexec_b64 s[2:3], s[2:3]
	v_mul_f32_e64 v71, |v1|, s65
	v_rndne_f32_e32 v73, v71
	v_cvt_i32_f32_e32 v72, v73
	v_fma_f32 v71, v73, s66, |v1|
	v_fmac_f32_e32 v71, 0xb3a22168, v73
	v_fmac_f32_e32 v71, 0xa7c234c4, v73
	s_or_b64 exec, exec, s[2:3]
	v_mul_f32_e32 v73, v71, v71
	v_mov_b32_e32 v74, 0x3c0881c4
	v_fmamk_f32 v74, v73, 0xb94c1982, v74
	v_fmaak_f32 v74, v73, v74, 0xbe2aaa9d
	v_mul_f32_e32 v74, v73, v74
	v_fmac_f32_e32 v71, v71, v74
	v_mov_b32_e32 v74, 0xbab64f3b
	v_fmamk_f32 v74, v73, 0x37d75334, v74
	v_fmaak_f32 v74, v73, v74, 0x3d2aabf7
	v_fmaak_f32 v74, v73, v74, 0xbf000004
	global_load_dwordx4 v[78:81], v[102:103], off offset:16
	global_load_dwordx4 v[90:93], v[102:103], off
	v_fma_f32 v73, v73, v74, 1.0
	v_lshlrev_b32_e32 v74, 30, v72
	v_and_b32_e32 v72, 1, v72
	v_cmp_eq_u32_e32 vcc, 0, v72
	v_xor_b32_e32 v70, v70, v1
	v_and_b32_e32 v75, 0x80000000, v74
	v_cndmask_b32_e32 v72, v73, v71, vcc
	v_xor_b32_e32 v71, 0x80000000, v71
	v_xor_b32_e32 v70, v70, v72
	v_cndmask_b32_e32 v71, v71, v73, vcc
	v_xor_b32_e32 v70, v70, v75
	v_bitop3_b32 v71, v71, v74, s67 bitop3:0x78
	v_cmp_class_f32_e64 vcc, v1, s68
	v_lshlrev_b32_e32 v250, 16, v82
	v_and_b32_e32 v251, 0xffff0000, v82
	v_cndmask_b32_e32 v98, v245, v71, vcc
	v_cndmask_b32_e32 v163, v245, v70, vcc
	global_load_dwordx4 v[70:73], v[102:103], off offset:48
	global_load_dwordx4 v[74:77], v[102:103], off offset:32
	v_lshlrev_b32_e32 v206, 16, v83
	v_and_b32_e32 v207, 0xffff0000, v83
	v_pk_mul_f32 v[82:83], v[250:251], v[250:251]
	v_pk_mul_f32 v[172:173], v[206:207], v[206:207]
	v_add_f32_e32 v1, v82, v83
	v_lshlrev_b32_e32 v204, 16, v84
	v_and_b32_e32 v205, 0xffff0000, v84
	v_add_f32_e32 v1, v172, v1
	v_lshlrev_b32_e32 v202, 16, v85
	v_and_b32_e32 v203, 0xffff0000, v85
	v_pk_mul_f32 v[84:85], v[204:205], v[204:205]
	v_add_f32_e32 v1, v173, v1
	v_add_f32_e32 v1, v84, v1
	v_pk_mul_f32 v[170:171], v[202:203], v[202:203]
	v_add_f32_e32 v1, v85, v1
	v_lshlrev_b32_e32 v200, 16, v86
	v_and_b32_e32 v201, 0xffff0000, v86
	v_add_f32_e32 v1, v170, v1
	v_lshlrev_b32_e32 v198, 16, v87
	v_and_b32_e32 v199, 0xffff0000, v87
	v_pk_mul_f32 v[86:87], v[200:201], v[200:201]
	v_add_f32_e32 v1, v171, v1
	v_add_f32_e32 v1, v86, v1
	v_pk_mul_f32 v[168:169], v[198:199], v[198:199]
	v_add_f32_e32 v1, v87, v1
	v_lshlrev_b32_e32 v196, 16, v88
	v_and_b32_e32 v197, 0xffff0000, v88
	v_add_f32_e32 v1, v168, v1
	v_lshlrev_b32_e32 v194, 16, v89
	v_and_b32_e32 v195, 0xffff0000, v89
	v_pk_mul_f32 v[88:89], v[196:197], v[196:197]
	v_add_f32_e32 v1, v169, v1
	v_add_f32_e32 v1, v88, v1
	v_pk_mul_f32 v[166:167], v[194:195], v[194:195]
	v_add_f32_e32 v1, v89, v1
	v_add_f32_e32 v1, v166, v1
	v_add_f32_e32 v1, v167, v1
	s_nop 1
	v_mov_b32_dpp v82, v1 quad_perm:[1,0,3,2] row_mask:0xf bank_mask:0xf
	ds_bpermute_b32 v192, v216, v98
	ds_bpermute_b32 v193, v216, v163
	ds_bpermute_b32 v190, v217, v98
	ds_bpermute_b32 v191, v217, v163
	s_waitcnt lgkmcnt(4)
	v_add_f32_e32 v1, v1, v82
	ds_bpermute_b32 v82, v209, v1
	ds_bpermute_b32 v188, v218, v98
	ds_bpermute_b32 v189, v218, v163
	ds_bpermute_b32 v186, v219, v98
	ds_bpermute_b32 v187, v219, v163
	s_waitcnt lgkmcnt(4)
	v_add_f32_e32 v1, v1, v82
	ds_bpermute_b32 v82, v210, v1
	ds_bpermute_b32 v184, v220, v98
	ds_bpermute_b32 v185, v220, v163
	ds_bpermute_b32 v182, v221, v98
	ds_bpermute_b32 v183, v221, v163
	s_waitcnt lgkmcnt(4)
	v_add_f32_e32 v1, v1, v82
	v_fmamk_f32 v1, v1, 0x3c000000, v95
	v_mul_f32_e32 v82, 0x4b800000, v1
	v_cmp_gt_f32_e32 vcc, s50, v1
	ds_bpermute_b32 v180, v222, v98
	ds_bpermute_b32 v181, v222, v163
	v_cndmask_b32_e32 v1, v1, v82, vcc
	v_rsq_f32_e32 v1, v1
	ds_bpermute_b32 v178, v223, v98
	ds_bpermute_b32 v179, v223, v163
	ds_bpermute_b32 v176, v224, v98
	v_mul_f32_e32 v82, 0x45800000, v1
	v_cndmask_b32_e32 v84, v1, v82, vcc
	v_mov_b32_e32 v85, v84
	v_pk_mul_f32 v[82:83], v[84:85], v[250:251] op_sel_hi:[0,1]
	s_waitcnt vmcnt(2)
	v_pk_mul_f32 v[82:83], v[90:91], v[82:83]
	ds_bpermute_b32 v177, v224, v163
	ds_bpermute_b32 v174, v225, v98
	ds_bpermute_b32 v175, v225, v163
	ds_bpermute_b32 v172, v226, v98
	ds_bpermute_b32 v173, v226, v163
	ds_bpermute_b32 v170, v227, v98
	ds_bpermute_b32 v171, v227, v163
	ds_bpermute_b32 v168, v228, v98
	ds_bpermute_b32 v169, v228, v163
	ds_bpermute_b32 v166, v229, v98
	ds_bpermute_b32 v167, v229, v163
	ds_bpermute_b32 v88, v230, v98
	ds_bpermute_b32 v89, v230, v163
	ds_bpermute_b32 v86, v231, v98
	ds_bpermute_b32 v87, v231, v163
	s_nop 1
	v_xor_b32_dpp v91, v82, v208 quad_perm:[1,0,3,2] row_mask:0xf bank_mask:0xf
	s_mov_b64 s[2:3], exec
	s_and_b64 exec, s[2:3], s[86:87]
	v_mov_b32_e32 v90, v82
	s_waitcnt lgkmcnt(0)
	v_pk_mul_f32 v[90:91], v[90:91], v[192:193]
	s_nop 0
	v_add_f32_e32 v82, v90, v91
	s_mov_b64 exec, s[2:3]
	s_waitcnt lgkmcnt(0)
	s_nop 1
	v_xor_b32_dpp v91, v83, v208 quad_perm:[1,0,3,2] row_mask:0xf bank_mask:0xf
	s_mov_b64 s[2:3], exec
	s_and_b64 exec, s[2:3], s[86:87]
	v_mov_b32_e32 v250, v83
	v_mov_b32_e32 v251, v191
	v_mov_b32_e32 v90, v190
	v_mul_f32_e32 v252, v83, v190
	s_waitcnt lgkmcnt(0)
	v_pk_fma_f32 v[90:91], v[250:251], v[90:91], v[252:253] op_sel_hi:[1,1,0]
	s_nop 0
	v_mov_b32_e32 v83, v91
	s_mov_b64 exec, s[2:3]
	s_waitcnt lgkmcnt(0)
	v_pk_mul_f32 v[90:91], v[84:85], v[206:207]
	v_pk_mul_f32 v[90:91], v[92:93], v[90:91]
	s_nop 1
	v_xor_b32_dpp v93, v90, v208 quad_perm:[1,0,3,2] row_mask:0xf bank_mask:0xf
	s_mov_b64 s[2:3], exec
	s_and_b64 exec, s[2:3], s[86:87]
	v_mov_b32_e32 v92, v90
	s_waitcnt lgkmcnt(0)
	v_pk_mul_f32 v[92:93], v[92:93], v[188:189]
	s_nop 0
	v_add_f32_e32 v90, v92, v93
	s_mov_b64 exec, s[2:3]
	s_waitcnt lgkmcnt(0)
	s_nop 1
	v_xor_b32_dpp v93, v91, v208 quad_perm:[1,0,3,2] row_mask:0xf bank_mask:0xf
	s_mov_b64 s[2:3], exec
	s_and_b64 exec, s[2:3], s[86:87]
	v_mov_b32_e32 v206, v91
	v_mov_b32_e32 v207, v187
	v_mov_b32_e32 v92, v186
	v_mul_f32_e32 v250, v91, v186
	s_waitcnt lgkmcnt(0)
	v_pk_fma_f32 v[92:93], v[206:207], v[92:93], v[250:251] op_sel_hi:[1,1,0]
	s_nop 0
	v_mov_b32_e32 v91, v93
	s_mov_b64 exec, s[2:3]
	s_waitcnt lgkmcnt(0)
	v_pk_mul_f32 v[92:93], v[84:85], v[204:205]
	v_pk_mul_f32 v[78:79], v[78:79], v[92:93]
	s_nop 1
	v_xor_b32_dpp v93, v78, v208 quad_perm:[1,0,3,2] row_mask:0xf bank_mask:0xf
	s_mov_b64 s[2:3], exec
	s_and_b64 exec, s[2:3], s[86:87]
	v_mov_b32_e32 v92, v78
	s_waitcnt lgkmcnt(0)
	v_pk_mul_f32 v[92:93], v[92:93], v[184:185]
	s_nop 0
	v_add_f32_e32 v78, v92, v93
	s_mov_b64 exec, s[2:3]
	s_waitcnt lgkmcnt(0)
	s_nop 1
	v_xor_b32_dpp v93, v79, v208 quad_perm:[1,0,3,2] row_mask:0xf bank_mask:0xf
	s_mov_b64 s[2:3], exec
	s_and_b64 exec, s[2:3], s[86:87]
	v_mov_b32_e32 v204, v79
	v_mov_b32_e32 v205, v183
	v_mov_b32_e32 v92, v182
	v_mul_f32_e32 v206, v79, v182
	s_waitcnt lgkmcnt(0)
	v_pk_fma_f32 v[92:93], v[204:205], v[92:93], v[206:207] op_sel_hi:[1,1,0]
	s_nop 0
	v_mov_b32_e32 v79, v93
	s_mov_b64 exec, s[2:3]
	s_waitcnt lgkmcnt(0)
	v_pk_mul_f32 v[92:93], v[84:85], v[202:203]
	v_pk_mul_f32 v[80:81], v[80:81], v[92:93]
	s_nop 1
	v_xor_b32_dpp v93, v80, v208 quad_perm:[1,0,3,2] row_mask:0xf bank_mask:0xf
	s_mov_b64 s[2:3], exec
	s_and_b64 exec, s[2:3], s[86:87]
	v_mov_b32_e32 v92, v80
	s_waitcnt lgkmcnt(0)
	v_pk_mul_f32 v[92:93], v[92:93], v[180:181]
	s_nop 0
	v_add_f32_e32 v80, v92, v93
	s_mov_b64 exec, s[2:3]
	s_waitcnt lgkmcnt(0)
	s_nop 1
	v_xor_b32_dpp v93, v81, v208 quad_perm:[1,0,3,2] row_mask:0xf bank_mask:0xf
	s_mov_b64 s[2:3], exec
	s_and_b64 exec, s[2:3], s[86:87]
	v_mov_b32_e32 v202, v81
	v_mov_b32_e32 v203, v179
	v_mov_b32_e32 v92, v178
	v_mul_f32_e32 v204, v81, v178
	s_waitcnt lgkmcnt(0)
	v_pk_fma_f32 v[92:93], v[202:203], v[92:93], v[204:205] op_sel_hi:[1,1,0]
	s_nop 0
	v_mov_b32_e32 v81, v93
	s_mov_b64 exec, s[2:3]
	s_waitcnt lgkmcnt(0)
	v_pk_mul_f32 v[92:93], v[84:85], v[200:201]
	s_waitcnt vmcnt(0)
	v_pk_mul_f32 v[74:75], v[74:75], v[92:93]
	s_nop 1
	v_xor_b32_dpp v93, v74, v208 quad_perm:[1,0,3,2] row_mask:0xf bank_mask:0xf
	s_mov_b64 s[2:3], exec
	s_and_b64 exec, s[2:3], s[86:87]
	v_mov_b32_e32 v92, v74
	s_waitcnt lgkmcnt(0)
	v_pk_mul_f32 v[92:93], v[92:93], v[176:177]
	s_nop 0
	v_add_f32_e32 v74, v92, v93
	s_mov_b64 exec, s[2:3]
	s_waitcnt lgkmcnt(0)
	s_nop 1
	v_xor_b32_dpp v93, v75, v208 quad_perm:[1,0,3,2] row_mask:0xf bank_mask:0xf
	s_mov_b64 s[2:3], exec
	s_and_b64 exec, s[2:3], s[86:87]
	v_mov_b32_e32 v200, v75
	v_mov_b32_e32 v201, v175
	v_mov_b32_e32 v92, v174
	v_mul_f32_e32 v202, v75, v174
	s_waitcnt lgkmcnt(0)
	v_pk_fma_f32 v[92:93], v[200:201], v[92:93], v[202:203] op_sel_hi:[1,1,0]
	s_nop 0
	v_mov_b32_e32 v75, v93
	s_mov_b64 exec, s[2:3]
	s_waitcnt lgkmcnt(0)
	v_pk_mul_f32 v[92:93], v[84:85], v[198:199]
	v_pk_mul_f32 v[76:77], v[92:93], v[76:77]
	s_nop 1
	v_xor_b32_dpp v93, v76, v208 quad_perm:[1,0,3,2] row_mask:0xf bank_mask:0xf
	s_mov_b64 s[2:3], exec
	s_and_b64 exec, s[2:3], s[86:87]
	v_mov_b32_e32 v92, v76
	s_waitcnt lgkmcnt(0)
	v_pk_mul_f32 v[92:93], v[92:93], v[172:173]
	s_nop 0
	v_add_f32_e32 v76, v92, v93
	s_mov_b64 exec, s[2:3]
	s_waitcnt lgkmcnt(0)
	s_nop 1
	v_xor_b32_dpp v93, v77, v208 quad_perm:[1,0,3,2] row_mask:0xf bank_mask:0xf
	s_mov_b64 s[2:3], exec
	s_and_b64 exec, s[2:3], s[86:87]
	v_mov_b32_e32 v198, v77
	v_mov_b32_e32 v199, v171
	v_mov_b32_e32 v92, v170
	v_mul_f32_e32 v200, v77, v170
	s_waitcnt lgkmcnt(0)
	v_pk_fma_f32 v[92:93], v[198:199], v[92:93], v[200:201] op_sel_hi:[1,1,0]
	s_nop 0
	v_mov_b32_e32 v77, v93
	s_mov_b64 exec, s[2:3]
	s_waitcnt lgkmcnt(0)
	v_pk_mul_f32 v[92:93], v[84:85], v[196:197]
	v_pk_mul_f32 v[70:71], v[92:93], v[70:71]
	s_nop 1
	v_xor_b32_dpp v93, v70, v208 quad_perm:[1,0,3,2] row_mask:0xf bank_mask:0xf
	s_mov_b64 s[2:3], exec
	s_and_b64 exec, s[2:3], s[86:87]
	v_mov_b32_e32 v92, v70
	s_waitcnt lgkmcnt(0)
	v_pk_mul_f32 v[92:93], v[92:93], v[168:169]
	s_nop 0
	v_add_f32_e32 v70, v92, v93
	s_mov_b64 exec, s[2:3]
	s_waitcnt lgkmcnt(0)
	s_nop 1
	v_xor_b32_dpp v93, v71, v208 quad_perm:[1,0,3,2] row_mask:0xf bank_mask:0xf
	s_mov_b64 s[2:3], exec
	s_and_b64 exec, s[2:3], s[86:87]
	v_mov_b32_e32 v196, v71
	v_mov_b32_e32 v197, v167
	v_mov_b32_e32 v92, v166
	v_mul_f32_e32 v198, v71, v166
	s_waitcnt lgkmcnt(0)
	v_pk_fma_f32 v[92:93], v[196:197], v[92:93], v[198:199] op_sel_hi:[1,1,0]
	s_nop 0
	v_mov_b32_e32 v71, v93
	s_mov_b64 exec, s[2:3]
	v_pk_mul_f32 v[84:85], v[84:85], v[194:195]
	v_pk_mul_f32 v[72:73], v[84:85], v[72:73]
	s_nop 1
	v_xor_b32_dpp v85, v72, v208 quad_perm:[1,0,3,2] row_mask:0xf bank_mask:0xf
	s_mov_b64 s[2:3], exec
	s_and_b64 exec, s[2:3], s[86:87]
	v_mov_b32_e32 v84, v72
	s_waitcnt lgkmcnt(0)
	v_pk_mul_f32 v[84:85], v[84:85], v[88:89]
	s_nop 0
	v_add_f32_e32 v72, v84, v85
	s_mov_b64 exec, s[2:3]
	s_waitcnt lgkmcnt(0)
	s_nop 1
	v_xor_b32_dpp v85, v73, v208 quad_perm:[1,0,3,2] row_mask:0xf bank_mask:0xf
	s_mov_b64 s[2:3], exec
	s_and_b64 exec, s[2:3], s[86:87]
	v_mov_b32_e32 v92, v73
	v_mov_b32_e32 v93, v87
	v_mov_b32_e32 v84, v86
	v_mul_f32_e32 v194, v73, v86
	s_waitcnt lgkmcnt(0)
	v_pk_fma_f32 v[84:85], v[92:93], v[84:85], v[194:195] op_sel_hi:[1,1,0]
	s_nop 0
	v_mov_b32_e32 v73, v85
	s_mov_b64 exec, s[2:3]
	v_lshl_add_u64 v[92:93], s[88:89], 0, v[146:147]
	v_cvt_pk_bf16_f32 v74, v74, v75
	v_cvt_pk_bf16_f32 v75, v76, v77
	v_cvt_pk_bf16_f32 v76, v70, v71
	v_add_co_u32_e32 v70, vcc, s69, v92
	v_cvt_pk_bf16_f32 v82, v82, v83
	v_cvt_pk_bf16_f32 v83, v90, v91
	v_cvt_pk_bf16_f32 v84, v78, v79
	s_waitcnt lgkmcnt(0)
	v_cvt_pk_bf16_f32 v85, v80, v81
	v_addc_co_u32_e32 v71, vcc, 0, v93, vcc
	v_cvt_pk_bf16_f32 v77, v72, v73
	global_store_dwordx4 v[70:71], v[82:85], off
	global_store_dwordx4 v[70:71], v[74:77], off offset:16
	global_load_dwordx4 v[82:85], v[104:105], off
	s_nop 0
	global_load_dwordx4 v[78:81], v[104:105], off offset:16
	global_load_dwordx4 v[70:73], v[104:105], off offset:48
	global_load_dwordx4 v[74:77], v[104:105], off offset:32
	v_lshlrev_b32_e32 v90, 16, v66
	v_and_b32_e32 v91, 0xffff0000, v66
	v_pk_mul_f32 v[92:93], v[90:91], v[90:91]
	v_lshlrev_b32_e32 v66, 16, v67
	v_and_b32_e32 v67, 0xffff0000, v67
	v_pk_mul_f32 v[202:203], v[66:67], v[66:67]
	v_add_f32_e32 v1, v92, v93
	v_lshlrev_b32_e32 v194, 16, v68
	v_and_b32_e32 v195, 0xffff0000, v68
	v_add_f32_e32 v1, v202, v1
	v_pk_mul_f32 v[204:205], v[194:195], v[194:195]
	v_add_f32_e32 v1, v203, v1
	v_lshlrev_b32_e32 v68, 16, v69
	v_and_b32_e32 v69, 0xffff0000, v69
	v_add_f32_e32 v1, v204, v1
	v_pk_mul_f32 v[206:207], v[68:69], v[68:69]
	v_add_f32_e32 v1, v205, v1
	v_lshlrev_b32_e32 v196, 16, v62
	v_and_b32_e32 v197, 0xffff0000, v62
	v_add_f32_e32 v1, v206, v1
	v_pk_mul_f32 v[250:251], v[196:197], v[196:197]
	v_add_f32_e32 v1, v207, v1
	v_lshlrev_b32_e32 v62, 16, v63
	v_and_b32_e32 v63, 0xffff0000, v63
	v_add_f32_e32 v1, v250, v1
	v_pk_mul_f32 v[252:253], v[62:63], v[62:63]
	v_add_f32_e32 v1, v251, v1
	v_lshlrev_b32_e32 v198, 16, v64
	v_and_b32_e32 v199, 0xffff0000, v64
	v_add_f32_e32 v1, v252, v1
	v_pk_mul_f32 v[240:241], v[198:199], v[198:199]
	v_add_f32_e32 v1, v253, v1
	v_lshlrev_b32_e32 v200, 16, v65
	v_and_b32_e32 v201, 0xffff0000, v65
	v_add_f32_e32 v1, v240, v1
	v_pk_mul_f32 v[64:65], v[200:201], v[200:201]
	v_add_f32_e32 v1, v241, v1
	v_add_f32_e32 v1, v64, v1
	v_add_f32_e32 v1, v65, v1
	s_nop 1
	v_mov_b32_dpp v64, v1 quad_perm:[1,0,3,2] row_mask:0xf bank_mask:0xf
	s_waitcnt lgkmcnt(0)
	v_add_f32_e32 v1, v1, v64
	ds_bpermute_b32 v64, v209, v1
	s_waitcnt lgkmcnt(0)
	v_add_f32_e32 v1, v1, v64
	ds_bpermute_b32 v64, v210, v1
	s_waitcnt lgkmcnt(0)
	v_add_f32_e32 v1, v1, v64
	v_fmamk_f32 v1, v1, 0x3c000000, v95
	v_mul_f32_e32 v64, 0x4b800000, v1
	v_cmp_gt_f32_e32 vcc, s50, v1
	s_nop 1
	v_cndmask_b32_e32 v1, v1, v64, vcc
	v_rsq_f32_e32 v1, v1
	s_nop 0
	v_mul_f32_e32 v64, 0x45800000, v1
	v_cndmask_b32_e32 v202, v1, v64, vcc
	v_mov_b32_e32 v203, v202
	v_pk_mul_f32 v[64:65], v[202:203], v[90:91] op_sel_hi:[0,1]
	v_pk_mul_f32 v[62:63], v[202:203], v[62:63]
	s_waitcnt vmcnt(3)
	v_pk_mul_f32 v[82:83], v[82:83], v[64:65]
	v_pk_mul_f32 v[64:65], v[202:203], v[66:67]
	s_nop 1
	v_xor_b32_dpp v93, v82, v208 quad_perm:[1,0,3,2] row_mask:0xf bank_mask:0xf
	v_pk_mul_f32 v[90:91], v[84:85], v[64:65]
	v_pk_mul_f32 v[64:65], v[202:203], v[194:195]
	s_waitcnt vmcnt(0)
	v_pk_mul_f32 v[66:67], v[62:63], v[76:77]
	v_pk_mul_f32 v[84:85], v[78:79], v[64:65]
	v_pk_mul_f32 v[64:65], v[202:203], v[68:69]
	v_pk_mul_f32 v[62:63], v[202:203], v[198:199]
	v_pk_mul_f32 v[78:79], v[80:81], v[64:65]
	v_pk_mul_f32 v[64:65], v[202:203], v[196:197]
	s_nop 0
	v_pk_mul_f32 v[68:69], v[74:75], v[64:65]
	v_pk_mul_f32 v[64:65], v[62:63], v[70:71]
	v_pk_mul_f32 v[62:63], v[202:203], v[200:201]
	s_nop 0
	v_pk_mul_f32 v[62:63], v[62:63], v[72:73]
	s_mov_b64 s[2:3], exec
	s_and_b64 exec, s[2:3], s[86:87]
	v_mov_b32_e32 v92, v82
	s_waitcnt lgkmcnt(0)
	v_pk_mul_f32 v[70:71], v[92:93], v[192:193]
	s_nop 0
	v_add_f32_e32 v82, v70, v71
	s_mov_b64 exec, s[2:3]
	s_nop 1
	v_xor_b32_dpp v71, v83, v208 quad_perm:[1,0,3,2] row_mask:0xf bank_mask:0xf
	s_mov_b64 s[2:3], exec
	s_and_b64 exec, s[2:3], s[86:87]
	v_mov_b32_e32 v70, v83
	v_mul_f32_e32 v72, v83, v190
	s_waitcnt lgkmcnt(0)
	v_pk_fma_f32 v[70:71], v[70:71], v[190:191], v[72:73] op_sel_hi:[1,1,0]
	s_nop 0
	v_mov_b32_e32 v83, v71
	s_mov_b64 exec, s[2:3]
	s_waitcnt lgkmcnt(0)
	s_nop 1
	v_xor_b32_dpp v71, v90, v208 quad_perm:[1,0,3,2] row_mask:0xf bank_mask:0xf
	s_mov_b64 s[2:3], exec
	s_and_b64 exec, s[2:3], s[86:87]
	v_mov_b32_e32 v70, v90
	s_waitcnt lgkmcnt(0)
	v_pk_mul_f32 v[70:71], v[70:71], v[188:189]
	s_nop 0
	v_add_f32_e32 v90, v70, v71
	s_mov_b64 exec, s[2:3]
	s_waitcnt lgkmcnt(0)
	s_nop 1
	v_xor_b32_dpp v71, v91, v208 quad_perm:[1,0,3,2] row_mask:0xf bank_mask:0xf
	s_mov_b64 s[2:3], exec
	s_and_b64 exec, s[2:3], s[86:87]
	v_mov_b32_e32 v70, v91
	s_waitcnt lgkmcnt(0)
	v_mul_f32_e32 v72, v71, v187
	v_pk_fma_f32 v[70:71], v[70:71], v[186:187], v[72:73] op_sel_hi:[1,1,0]
	s_nop 0
	v_mov_b32_e32 v91, v70
	s_mov_b64 exec, s[2:3]
	s_waitcnt lgkmcnt(0)
	s_nop 1
	v_xor_b32_dpp v71, v84, v208 quad_perm:[1,0,3,2] row_mask:0xf bank_mask:0xf
	s_mov_b64 s[2:3], exec
	s_and_b64 exec, s[2:3], s[86:87]
	v_mov_b32_e32 v70, v84
	s_waitcnt lgkmcnt(0)
	v_pk_mul_f32 v[70:71], v[70:71], v[184:185]
	s_nop 0
	v_add_f32_e32 v84, v70, v71
	s_mov_b64 exec, s[2:3]
	s_waitcnt lgkmcnt(0)
	s_nop 1
	v_xor_b32_dpp v71, v85, v208 quad_perm:[1,0,3,2] row_mask:0xf bank_mask:0xf
	s_mov_b64 s[2:3], exec
	s_and_b64 exec, s[2:3], s[86:87]
	v_mov_b32_e32 v70, v85
	s_waitcnt lgkmcnt(0)
	v_mul_f32_e32 v72, v71, v183
	v_pk_fma_f32 v[70:71], v[70:71], v[182:183], v[72:73] op_sel_hi:[1,1,0]
	s_nop 0
	v_mov_b32_e32 v85, v70
	s_mov_b64 exec, s[2:3]
	s_waitcnt lgkmcnt(0)
	s_nop 1
	v_xor_b32_dpp v71, v78, v208 quad_perm:[1,0,3,2] row_mask:0xf bank_mask:0xf
	s_mov_b64 s[2:3], exec
	s_and_b64 exec, s[2:3], s[86:87]
	v_mov_b32_e32 v70, v78
	s_waitcnt lgkmcnt(0)
	v_pk_mul_f32 v[70:71], v[70:71], v[180:181]
	s_nop 0
	v_add_f32_e32 v78, v70, v71
	s_mov_b64 exec, s[2:3]
	s_waitcnt lgkmcnt(0)
	s_nop 1
	v_xor_b32_dpp v71, v79, v208 quad_perm:[1,0,3,2] row_mask:0xf bank_mask:0xf
	s_mov_b64 s[2:3], exec
	s_and_b64 exec, s[2:3], s[86:87]
	v_mov_b32_e32 v70, v79
	s_waitcnt lgkmcnt(0)
	v_mul_f32_e32 v72, v71, v179
	v_pk_fma_f32 v[70:71], v[70:71], v[178:179], v[72:73] op_sel_hi:[1,1,0]
	s_nop 0
	v_mov_b32_e32 v79, v70
	s_mov_b64 exec, s[2:3]
	s_waitcnt lgkmcnt(0)
	s_nop 1
	v_xor_b32_dpp v71, v68, v208 quad_perm:[1,0,3,2] row_mask:0xf bank_mask:0xf
	s_mov_b64 s[2:3], exec
	s_and_b64 exec, s[2:3], s[86:87]
	v_mov_b32_e32 v70, v68
	s_waitcnt lgkmcnt(0)
	v_pk_mul_f32 v[70:71], v[70:71], v[176:177]
	s_nop 0
	v_add_f32_e32 v68, v70, v71
	s_mov_b64 exec, s[2:3]
	s_waitcnt lgkmcnt(0)
	s_nop 1
	v_xor_b32_dpp v71, v69, v208 quad_perm:[1,0,3,2] row_mask:0xf bank_mask:0xf
	s_mov_b64 s[2:3], exec
	s_and_b64 exec, s[2:3], s[86:87]
	v_mov_b32_e32 v70, v69
	s_waitcnt lgkmcnt(0)
	v_mul_f32_e32 v72, v71, v175
	v_pk_fma_f32 v[70:71], v[70:71], v[174:175], v[72:73] op_sel_hi:[1,1,0]
	s_nop 0
	v_mov_b32_e32 v69, v70
	s_mov_b64 exec, s[2:3]
	s_waitcnt lgkmcnt(0)
	s_nop 1
	v_xor_b32_dpp v71, v66, v208 quad_perm:[1,0,3,2] row_mask:0xf bank_mask:0xf
	s_mov_b64 s[2:3], exec
	s_and_b64 exec, s[2:3], s[86:87]
	v_mov_b32_e32 v70, v66
	s_waitcnt lgkmcnt(0)
	v_pk_mul_f32 v[70:71], v[70:71], v[172:173]
	s_nop 0
	v_add_f32_e32 v66, v70, v71
	s_mov_b64 exec, s[2:3]
	s_waitcnt lgkmcnt(0)
	s_nop 1
	v_xor_b32_dpp v71, v67, v208 quad_perm:[1,0,3,2] row_mask:0xf bank_mask:0xf
	s_mov_b64 s[2:3], exec
	s_and_b64 exec, s[2:3], s[86:87]
	v_mov_b32_e32 v70, v67
	s_waitcnt lgkmcnt(0)
	v_mul_f32_e32 v72, v71, v171
	v_pk_fma_f32 v[70:71], v[70:71], v[170:171], v[72:73] op_sel_hi:[1,1,0]
	s_nop 0
	v_mov_b32_e32 v67, v70
	s_mov_b64 exec, s[2:3]
	s_waitcnt lgkmcnt(0)
	s_nop 1
	v_xor_b32_dpp v71, v64, v208 quad_perm:[1,0,3,2] row_mask:0xf bank_mask:0xf
	s_mov_b64 s[2:3], exec
	s_and_b64 exec, s[2:3], s[86:87]
	v_mov_b32_e32 v70, v64
	s_waitcnt lgkmcnt(0)
	v_pk_mul_f32 v[70:71], v[70:71], v[168:169]
	s_nop 0
	v_add_f32_e32 v64, v70, v71
	s_mov_b64 exec, s[2:3]
	s_waitcnt lgkmcnt(0)
	s_nop 1
	v_xor_b32_dpp v71, v65, v208 quad_perm:[1,0,3,2] row_mask:0xf bank_mask:0xf
	s_mov_b64 s[2:3], exec
	s_and_b64 exec, s[2:3], s[86:87]
	v_mov_b32_e32 v70, v65
	s_waitcnt lgkmcnt(0)
	v_mul_f32_e32 v72, v71, v167
	v_pk_fma_f32 v[70:71], v[70:71], v[166:167], v[72:73] op_sel_hi:[1,1,0]
	s_nop 0
	v_mov_b32_e32 v65, v70
	s_mov_b64 exec, s[2:3]
	s_waitcnt lgkmcnt(0)
	s_nop 1
	v_xor_b32_dpp v71, v62, v208 quad_perm:[1,0,3,2] row_mask:0xf bank_mask:0xf
	s_mov_b64 s[2:3], exec
	s_and_b64 exec, s[2:3], s[86:87]
	v_mov_b32_e32 v70, v62
	s_waitcnt lgkmcnt(0)
	v_pk_mul_f32 v[70:71], v[70:71], v[88:89]
	s_nop 0
	v_add_f32_e32 v62, v70, v71
	s_mov_b64 exec, s[2:3]
	s_waitcnt lgkmcnt(0)
	s_nop 1
	v_mov_b32_dpp v71, v63 quad_perm:[1,0,3,2] row_mask:0xf bank_mask:0xf
	v_cmp_lt_i32_e32 vcc, 0, v96
	s_and_saveexec_b64 s[2:3], vcc
	s_xor_b64 s[2:3], exec, s[2:3]
	s_cbranch_execz .LBB0_755
	v_cmp_eq_u32_e32 vcc, 1, v96
	s_and_saveexec_b64 s[10:11], vcc
	s_cbranch_execz .LBB0_752
	v_mov_b32_e32 v70, v63
	s_waitcnt lgkmcnt(0)
	v_mul_f32_e32 v72, v71, v87
	v_pk_fma_f32 v[70:71], v[70:71], v[86:87], v[72:73] op_sel_hi:[1,1,0]
	s_nop 0
	v_mov_b32_e32 v63, v70

.LBB0_759:
	s_or_b64 exec, exec, s[2:3]
	v_lshlrev_b32_e32 v74, 16, v50
	ds_bpermute_b32 v76, v232, v98
	ds_bpermute_b32 v75, v232, v163
	ds_bpermute_b32 v72, v233, v98
	ds_bpermute_b32 v73, v233, v163
	ds_bpermute_b32 v70, v234, v98
	ds_bpermute_b32 v63, v234, v163
	ds_bpermute_b32 v68, v235, v98
	ds_bpermute_b32 v69, v235, v163
	ds_bpermute_b32 v66, v236, v98
	ds_bpermute_b32 v65, v236, v163
	ds_bpermute_b32 v60, v237, v98
	ds_bpermute_b32 v61, v237, v163
	ds_bpermute_b32 v58, v238, v98
	ds_bpermute_b32 v57, v238, v163
	ds_bpermute_b32 v54, v239, v98
	ds_bpermute_b32 v55, v239, v163
	s_nop 1
	v_xor_b32_dpp v77, v74, v208 quad_perm:[1,0,3,2] row_mask:0xf bank_mask:0xf
	v_and_b32_e32 v1, 0xffff0000, v50
	s_mov_b64 s[2:3], exec
	s_and_b64 exec, s[2:3], s[86:87]
	s_waitcnt lgkmcnt(0)
	v_pk_mul_f32 v[74:75], v[74:75], v[76:77]
	s_nop 0
	v_add_f32_e32 v74, v74, v75
	s_mov_b64 exec, s[2:3]
	s_waitcnt lgkmcnt(13)
	s_nop 1
	v_xor_b32_dpp v75, v1, v208 quad_perm:[1,0,3,2] row_mask:0xf bank_mask:0xf
	v_mov_b32_e32 v50, v74
	s_mov_b64 s[2:3], exec
	s_and_b64 exec, s[2:3], s[86:87]
	v_mov_b32_e32 v76, v1
	s_waitcnt lgkmcnt(0)
	v_mov_b32_e32 v77, v73
	s_waitcnt lgkmcnt(0)
	v_mov_b32_e32 v73, v75
	v_mul_f32_e32 v56, v1, v72
	v_pk_fma_f32 v[72:73], v[76:77], v[72:73], v[56:57] op_sel_hi:[1,1,0]
	s_nop 0
	v_mov_b32_e32 v1, v73
	s_mov_b64 exec, s[2:3]
	v_lshlrev_b32_e32 v62, 16, v51
	s_nop 1
	v_xor_b32_dpp v71, v62, v208 quad_perm:[1,0,3,2] row_mask:0xf bank_mask:0xf
	v_and_b32_e32 v51, 0xffff0000, v51
	s_mov_b64 s[2:3], exec
	s_and_b64 exec, s[2:3], s[86:87]
	s_waitcnt lgkmcnt(0)
	v_pk_mul_f32 v[62:63], v[70:71], v[62:63]
	s_nop 0
	v_add_f32_e32 v62, v62, v63
	s_mov_b64 exec, s[2:3]
	s_waitcnt lgkmcnt(0)
	s_nop 1
	v_xor_b32_dpp v71, v51, v208 quad_perm:[1,0,3,2] row_mask:0xf bank_mask:0xf
	s_mov_b64 s[2:3], exec
	s_and_b64 exec, s[2:3], s[86:87]
	v_mov_b32_e32 v72, v51
	v_mov_b32_e32 v73, v69
	s_waitcnt lgkmcnt(0)
	v_mov_b32_e32 v69, v71
	v_mul_f32_e32 v56, v51, v68
	v_pk_fma_f32 v[68:69], v[72:73], v[68:69], v[56:57] op_sel_hi:[1,1,0]
	s_nop 0
	v_mov_b32_e32 v51, v69
	s_mov_b64 exec, s[2:3]
	v_lshlrev_b32_e32 v64, 16, v52
	s_nop 1
	v_xor_b32_dpp v67, v64, v208 quad_perm:[1,0,3,2] row_mask:0xf bank_mask:0xf
	v_and_b32_e32 v63, 0xffff0000, v52
	s_mov_b64 s[2:3], exec
	s_and_b64 exec, s[2:3], s[86:87]
	s_waitcnt lgkmcnt(0)
	v_pk_mul_f32 v[64:65], v[66:67], v[64:65]
	s_nop 0
	v_add_f32_e32 v64, v64, v65
	s_mov_b64 exec, s[2:3]
	s_waitcnt lgkmcnt(0)
	s_nop 1
	v_xor_b32_dpp v67, v63, v208 quad_perm:[1,0,3,2] row_mask:0xf bank_mask:0xf
	s_mov_b64 s[2:3], exec
	s_and_b64 exec, s[2:3], s[86:87]
	v_mov_b32_e32 v68, v63
	v_mov_b32_e32 v69, v61
	s_waitcnt lgkmcnt(0)
	v_mov_b32_e32 v61, v67
	v_mul_f32_e32 v52, v63, v60
	v_pk_fma_f32 v[60:61], v[68:69], v[60:61], v[52:53] op_sel_hi:[1,1,0]
	s_nop 0
	v_mov_b32_e32 v63, v61
	s_mov_b64 exec, s[2:3]
	v_lshlrev_b32_e32 v56, 16, v53
	s_nop 1
	v_xor_b32_dpp v59, v56, v208 quad_perm:[1,0,3,2] row_mask:0xf bank_mask:0xf
	v_and_b32_e32 v53, 0xffff0000, v53
	s_mov_b64 s[2:3], exec
	s_and_b64 exec, s[2:3], s[86:87]
	s_waitcnt lgkmcnt(0)
	v_pk_mul_f32 v[56:57], v[58:59], v[56:57]
	s_nop 0
	v_add_f32_e32 v56, v56, v57
	s_mov_b64 exec, s[2:3]
	s_waitcnt lgkmcnt(0)
	s_nop 1
	v_mov_b32_dpp v59, v53 quad_perm:[1,0,3,2] row_mask:0xf bank_mask:0xf
	s_mov_b64 s[2:3], exec
	s_and_b64 exec, s[2:3], s[82:83]
	v_mov_b32_e32 v60, v53
	v_mov_b32_e32 v61, v55
	s_waitcnt lgkmcnt(0)
	v_mov_b32_e32 v55, v59
	v_mul_f32_e32 v52, v53, v54
	v_pk_fma_f32 v[52:53], v[60:61], v[54:55], v[52:53] op_sel_hi:[1,1,0]
	s_and_b64 exec, s[2:3], s[84:85]
	v_mov_b32_e32 v58, v53
	v_mul_f32_e32 v52, v53, v54
	s_waitcnt lgkmcnt(0)
	v_pk_fma_f32 v[52:53], v[58:59], v[54:55], v[52:53] op_sel_hi:[1,1,0] neg_lo:[1,0,0] neg_hi:[1,0,0]
	s_mov_b64 exec, s[2:3]
	v_lshl_add_u64 v[54:55], s[88:89], 0, v[154:155]
	v_cvt_pk_bf16_f32 v50, v50, v1
	v_cvt_pk_bf16_f32 v51, v62, v51
	v_cvt_pk_bf16_f32 v52, v64, v63
	v_cvt_pk_bf16_f32 v53, v56, v53
	global_store_dwordx4 v[54:55], v[50:53], off
	global_load_dword v1, v[106:107], off
	v_and_or_b32 v56, v94, 15, v215
	v_mul_f32_e32 v50, v249, v249
	ds_bpermute_b32 v50, v211, v50
	v_ashrrev_i32_e32 v52, 4, v94
	s_waitcnt lgkmcnt(0)
	v_fmac_f32_e32 v50, v249, v249
	ds_bpermute_b32 v51, v212, v50
	s_waitcnt lgkmcnt(0)
	v_add_f32_e32 v50, v50, v51
	ds_bpermute_b32 v51, v213, v50
	s_waitcnt lgkmcnt(0)
	v_add_f32_e32 v50, v50, v51
	ds_bpermute_b32 v51, v210, v50
	s_waitcnt lgkmcnt(0)
	v_add_f32_e32 v50, v50, v51
	ds_bpermute_b32 v51, v209, v50
	s_waitcnt lgkmcnt(0)
	v_add_f32_e32 v53, v50, v51
	s_nop 1
	v_mov_b32_dpp v54, v53 quad_perm:[1,0,3,2] row_mask:0xf bank_mask:0xf
	ds_bpermute_b32 v50, v214, v98
	ds_bpermute_b32 v51, v214, v163
	v_lshlrev_b32_e32 v98, 4, v56
	v_mov_b32_e32 v163, v99
	s_waitcnt lgkmcnt(2)
	v_add_f32_e32 v53, v53, v54
	v_fmamk_f32 v53, v53, 0x3c800000, v95
	v_mul_f32_e32 v54, 0x4b800000, v53
	v_cmp_gt_f32_e32 vcc, s50, v53
	s_nop 1
	v_cndmask_b32_e32 v53, v53, v54, vcc
	v_rsq_f32_e32 v54, v53
	v_ashrrev_i32_e32 v53, 31, v52
	v_lshlrev_b64 v[52:53], 11, v[52:53]
	v_lshl_add_u64 v[52:53], v[100:101], 0, v[52:53]
	v_mul_f32_e32 v55, 0x45800000, v54
	v_cndmask_b32_e32 v54, v54, v55, vcc
	v_mul_f32_e32 v54, v249, v54
	v_lshl_add_u64 v[52:53], v[52:53], 0, v[98:99]
	s_waitcnt vmcnt(0)
	v_mul_f32_e32 v54, v1, v54
	ds_bpermute_b32 v55, v213, v54
	s_waitcnt lgkmcnt(0)
	v_pk_mul_f32 v[50:51], v[54:55], v[50:51]
	s_nop 0
	v_sub_f32_e32 v1, v50, v51
	v_add_f32_e32 v50, v51, v50
	v_cndmask_b32_e64 v50, v54, v50, s[0:1]
	v_cndmask_b32_e64 v1, v50, v1, s[6:7]
	v_cvt_pk_bf16_f32 v1, v1, s0
	v_lshl_add_u64 v[50:51], v[52:53], 0, v[162:163]
	global_store_short v[50:51], v1, off
	s_and_saveexec_b64 s[2:3], s[6:7]
	s_cbranch_execz .LBB0_809
	v_mul_f32_e32 v1, 0x3d3504f3, v248
	v_lshl_add_u64 v[50:51], s[88:89], 0, v[140:141]
	global_store_dword v[50:51], v1, off
